# baseline (speedup 1.0000x reference)
.LBB1_13:
	v_mfma_f32_32x32x16_bf16 v[2:17], v[78:81], v[206:209], v[236:251]
	ds_read_b128 v[174:177], v210
	v_add_u32_e32 v195, v230, v228
	v_mfma_f32_32x32x16_bf16 v[2:17], v[74:77], v[190:193], v[2:17]
	ds_read_b128 v[170:173], v210 offset:1024
	v_exp_f32_e32 v199, v28
	v_exp_f32_e32 v198, v32
	v_exp_f32_e32 v197, v20
	v_exp_f32_e32 v196, v24
	v_mfma_f32_32x32x16_bf16 v[2:17], v[70:73], v[158:161], v[2:17]
	ds_read_b128 v[166:169], v210 offset:2048
	v_exp_f32_e32 v18, v18
	v_exp_f32_e32 v22, v22
	v_exp_f32_e32 v24, v26
	v_exp_f32_e32 v26, v30
	v_fma_f32 v20, v197, s12, s12
	v_fma_f32 v28, v196, s12, s12
	v_fma_f32 v30, v199, s12, s12
	v_fma_f32 v32, v198, s12, s12
	v_mfma_f32_32x32x16_bf16 v[2:17], v[66:69], v[142:145], v[2:17]
	ds_read_b128 v[162:165], v210 offset:3072
	v_exp_f32_e32 v19, v19
	v_exp_f32_e32 v23, v23
	v_exp_f32_e32 v27, v27
	v_exp_f32_e32 v31, v31
	v_fmac_f32_e32 v20, v18, v20
	v_fmac_f32_e32 v28, v22, v28
	v_fmac_f32_e32 v30, v24, v30
	v_fmac_f32_e32 v32, v26, v32
	v_mfma_f32_32x32x16_bf16 v[2:17], v[62:65], v[154:157], v[2:17]
	ds_read_b128 v[158:161], v210 offset:4096
	v_add_f32_e32 v22, 1.0, v19
	v_rcp_f32_e32 v19, v20
	v_rcp_f32_e32 v18, v28
	v_add_f32_e32 v20, 1.0, v23
	v_rcp_f32_e32 v191, v30
	v_rcp_f32_e32 v190, v32
	v_mfma_f32_32x32x16_bf16 v[2:17], v[58:61], v[182:185], v[2:17]
	ds_read_b128 v[154:157], v210 offset:5120
	v_exp_f32_e32 v206, v21
	v_exp_f32_e32 v207, v25
	v_add_f32_e32 v23, 1.0, v27
	v_rcp_f32_e32 v192, v20
	v_add_f32_e32 v20, 1.0, v31
	v_rcp_f32_e32 v193, v22
	v_mfma_f32_32x32x16_bf16 v[2:17], v[54:57], v[186:189], v[2:17]
	ds_read_b128 v[142:145], v210 offset:6144
	v_exp_f32_e32 v208, v29
	v_exp_f32_e32 v209, v33
	v_rcp_f32_e32 v183, v23
	v_rcp_f32_e32 v182, v20
	v_mfma_f32_32x32x16_bf16 v[2:17], v[50:53], v[134:137], v[2:17]
	ds_read_b128 v[130:133], v210 offset:7168
	v_fma_f32 v186, -v196, v18, v18
	v_fma_f32 v187, -v197, v19, v19
	ds_read_b128 v[18:21], v231 offset:36928
	ds_read_b128 v[22:25], v231 offset:36944
	ds_read_b128 v[26:29], v231 offset:36960
	ds_read_b128 v[30:33], v231 offset:36976
	v_pk_fma_f32 v[200:201], v[192:193], v[220:221], v[186:187]
	v_pk_fma_f32 v[134:135], v[198:199], v[190:191], v[190:191] neg_lo:[1,0,0] neg_hi:[1,0,0]
	s_nop 0
	v_pk_fma_f32 v[198:199], v[182:183], v[222:223], v[134:135]
	v_mfma_f32_32x32x16_bf16 v[2:17], v[46:49], v[138:141], v[2:17]
	ds_read_b128 v[134:137], v195 offset:16384
	v_add_f32_e32 v182, 1.0, v206
	v_exp_f32_e32 v183, v201
	v_exp_f32_e32 v186, v200
	v_exp_f32_e32 v187, v199
	v_exp_f32_e32 v188, v198
	v_add_f32_e32 v189, 1.0, v207
	v_add_f32_e32 v190, 1.0, v208
	v_add_f32_e32 v191, 1.0, v209
	v_mfma_f32_32x32x16_bf16 v[2:17], v[42:45], v[146:149], v[2:17]
	ds_read_b128 v[138:141], v195 offset:16416
	v_fmac_f32_e32 v182, v182, v183
	v_fmac_f32_e32 v189, v189, v186
	v_fmac_f32_e32 v190, v190, v187
	v_fmac_f32_e32 v191, v191, v188
	v_mfma_f32_32x32x16_bf16 v[2:17], v[38:41], v[150:153], v[2:17]
	ds_read_b128 v[146:149], v195 offset:16448
	v_rcp_f32_e32 v182, v182
	v_rcp_f32_e32 v189, v189
	v_mfma_f32_32x32x16_bf16 v[2:17], v[34:37], v[178:181], v[2:17]
	ds_read_b128 v[150:153], v195 offset:16480
	v_rcp_f32_e32 v190, v190
	v_rcp_f32_e32 v191, v191
	v_fma_f32 v182, -v183, v182, v182
	v_fma_f32 v183, -v186, v189, v189
	s_waitcnt lgkmcnt(4)
	v_mfma_f32_32x32x16_bf16 v[18:33], v[126:129], v[174:177], v[18:33]
	v_fma_f32 v186, -v187, v190, v190
	v_fma_f32 v187, -v188, v191, v191
	v_cvt_pk_bf16_f32 v252, v182, v183
	v_cvt_pk_bf16_f32 v253, v186, v187
	v_mfma_f32_32x32x16_bf16 v[18:33], v[122:125], v[170:173], v[18:33]
	s_nop 1
	v_exp_f32_e32 v179, v4
	v_exp_f32_e32 v178, v8
	v_exp_f32_e32 v181, v12
	v_exp_f32_e32 v180, v16
	v_mfma_f32_32x32x16_bf16 v[18:33], v[118:121], v[166:169], v[18:33]
	v_exp_f32_e32 v2, v2
	v_exp_f32_e32 v6, v6
	v_exp_f32_e32 v10, v10
	v_exp_f32_e32 v12, v14
	v_fma_f32 v4, v179, s12, s12
	v_fma_f32 v8, v178, s12, s12
	v_fma_f32 v14, v181, s12, s12
	v_fma_f32 v16, v180, s12, s12
	v_mfma_f32_32x32x16_bf16 v[18:33], v[114:117], v[162:165], v[18:33]
	v_exp_f32_e32 v3, v3
	v_fmac_f32_e32 v4, v2, v4
	v_exp_f32_e32 v2, v7
	v_fmac_f32_e32 v8, v6, v8
	v_exp_f32_e32 v6, v11
	v_exp_f32_e32 v7, v15
	v_fmac_f32_e32 v14, v10, v14
	v_fmac_f32_e32 v16, v12, v16
	v_mfma_f32_32x32x16_bf16 v[18:33], v[110:113], v[158:161], v[18:33]
	v_add_f32_e32 v10, 1.0, v3
	v_rcp_f32_e32 v3, v4
	v_add_f32_e32 v4, 1.0, v2
	v_rcp_f32_e32 v2, v8
	v_rcp_f32_e32 v183, v14
	v_rcp_f32_e32 v182, v16
	v_mfma_f32_32x32x16_bf16 v[18:33], v[106:109], v[154:157], v[18:33]
	v_add_f32_e32 v6, 1.0, v6
	v_add_f32_e32 v7, 1.0, v7
	v_rcp_f32_e32 v187, v10
	v_rcp_f32_e32 v186, v4
	v_exp_f32_e32 v190, v5
	v_exp_f32_e32 v191, v9
	v_mfma_f32_32x32x16_bf16 v[18:33], v[102:105], v[142:145], v[18:33]
	v_rcp_f32_e32 v189, v6
	v_rcp_f32_e32 v188, v7
	v_exp_f32_e32 v192, v13
	v_exp_f32_e32 v193, v17
	v_mfma_f32_32x32x16_bf16 v[18:33], v[98:101], v[130:133], v[18:33]
	v_fma_f32 v178, -v178, v2, v2
	v_fma_f32 v179, -v179, v3, v3
	v_pk_fma_f32 v[206:207], v[186:187], v[216:217], v[178:179]
	s_nop 0
	v_pk_fma_f32 v[178:179], v[180:181], v[182:183], v[182:183] neg_lo:[1,0,0] neg_hi:[1,0,0]
	s_nop 0
	v_pk_fma_f32 v[208:209], v[188:189], v[218:219], v[178:179]
	s_waitcnt lgkmcnt(0)
	v_mfma_f32_32x32x16_bf16 v[18:33], v[94:97], v[134:137], v[18:33]
	v_add_f32_e32 v178, 1.0, v190
	v_exp_f32_e32 v179, v207
	v_add_f32_e32 v180, 1.0, v191
	v_exp_f32_e32 v181, v206
	v_exp_f32_e32 v182, v209
	v_exp_f32_e32 v183, v208
	v_add_f32_e32 v184, 1.0, v192
	v_add_f32_e32 v185, 1.0, v193
	v_mfma_f32_32x32x16_bf16 v[18:33], v[90:93], v[138:141], v[18:33]
	v_fmac_f32_e32 v178, v178, v179
	v_fmac_f32_e32 v180, v180, v181
	v_fmac_f32_e32 v184, v184, v182
	v_fmac_f32_e32 v185, v185, v183
	v_rcp_f32_e32 v178, v178
	v_rcp_f32_e32 v180, v180
	v_mfma_f32_32x32x16_bf16 v[18:33], v[86:89], v[146:149], v[18:33]
	v_rcp_f32_e32 v184, v184
	v_rcp_f32_e32 v185, v185
	v_fma_f32 v178, -v179, v178, v178
	v_fma_f32 v179, -v181, v180, v180
	v_mfma_f32_32x32x16_bf16 v[18:33], v[82:85], v[150:153], v[18:33]
	v_fma_f32 v180, -v182, v184, v184
	v_fma_f32 v181, -v183, v185, v185
	v_cvt_pk_bf16_f32 v254, v178, v179
	v_cvt_pk_bf16_f32 v255, v180, v181
	ds_write_b128 v211, v[252:255] offset:8192
	s_waitcnt lgkmcnt(0)
	s_barrier
	s_add_i32 s1, s1, 2
	s_cmp_gt_u32 s1, 16
	v_add_u32_e32 v232, 0x200, v232
	s_cbranch_scc1 .LBB1_30
.LBB1_14:
	v_mfma_f32_32x32x16_bf16 v[2:17], v[78:81], v[174:177], v[236:251]
	v_add_u32_e32 v192, v230, v229
	ds_read2_b32 v[228:229], v232 offset1:32
	ds_read_b128 v[194:197], v210 offset:8192
	v_mfma_f32_32x32x16_bf16 v[2:17], v[74:77], v[170:173], v[2:17]
	ds_read_b128 v[178:181], v210 offset:9216
	v_exp_f32_e32 v187, v20
	v_exp_f32_e32 v186, v24
	v_exp_f32_e32 v189, v28
	v_exp_f32_e32 v188, v32
	v_mfma_f32_32x32x16_bf16 v[2:17], v[70:73], v[166:169], v[2:17]
	ds_read_b128 v[170:173], v210 offset:10240
	v_exp_f32_e32 v18, v18
	v_exp_f32_e32 v22, v22
	v_exp_f32_e32 v24, v26
	v_exp_f32_e32 v26, v30
	v_fma_f32 v20, v187, s12, s12
	v_fma_f32 v28, v186, s12, s12
	v_fma_f32 v30, v189, s12, s12
	v_fma_f32 v32, v188, s12, s12
	v_mfma_f32_32x32x16_bf16 v[2:17], v[66:69], v[162:165], v[2:17]
	ds_read_b128 v[166:169], v210 offset:11264
	v_exp_f32_e32 v19, v19
	v_exp_f32_e32 v23, v23
	v_exp_f32_e32 v27, v27
	v_exp_f32_e32 v31, v31
	v_fmac_f32_e32 v20, v18, v20
	v_fmac_f32_e32 v28, v22, v28
	v_fmac_f32_e32 v30, v24, v30
	v_fmac_f32_e32 v32, v26, v32
	v_mfma_f32_32x32x16_bf16 v[2:17], v[62:65], v[158:161], v[2:17]
	ds_read_b128 v[162:165], v210 offset:12288
	v_add_f32_e32 v22, 1.0, v19
	v_rcp_f32_e32 v19, v20
	v_rcp_f32_e32 v18, v28
	v_rcp_f32_e32 v191, v30
	v_rcp_f32_e32 v190, v32
	v_add_f32_e32 v20, 1.0, v23
	v_mfma_f32_32x32x16_bf16 v[2:17], v[58:61], v[154:157], v[2:17]
	ds_read_b128 v[174:177], v210 offset:13312
	v_rcp_f32_e32 v159, v22
	v_rcp_f32_e32 v158, v20
	v_exp_f32_e32 v160, v21
	v_exp_f32_e32 v161, v25
	v_add_f32_e32 v23, 1.0, v27
	v_add_f32_e32 v20, 1.0, v31
	v_mfma_f32_32x32x16_bf16 v[2:17], v[54:57], v[142:145], v[2:17]
	ds_read_b128 v[182:185], v210 offset:14336
	v_rcp_f32_e32 v155, v23
	v_rcp_f32_e32 v154, v20
	v_exp_f32_e32 v193, v29
	v_exp_f32_e32 v217, v33
	v_mfma_f32_32x32x16_bf16 v[2:17], v[50:53], v[130:133], v[2:17]
	ds_read_b128 v[142:145], v210 offset:15360
	v_fma_f32 v156, -v186, v18, v18
	v_fma_f32 v157, -v187, v19, v19
	ds_read_b128 v[18:21], v231 offset:36928
	ds_read_b128 v[22:25], v231 offset:36944
	ds_read_b128 v[26:29], v231 offset:36960
	ds_read_b128 v[30:33], v231 offset:36976
	v_pk_fma_f32 v[214:215], v[158:159], v[214:215], v[156:157]
	v_pk_fma_f32 v[130:131], v[188:189], v[190:191], v[190:191] neg_lo:[1,0,0] neg_hi:[1,0,0]
	s_nop 0
	v_pk_fma_f32 v[212:213], v[154:155], v[212:213], v[130:131]
	v_mfma_f32_32x32x16_bf16 v[2:17], v[46:49], v[134:137], v[2:17]
	ds_read_b128 v[154:157], v192 offset:16384
	v_add_f32_e32 v130, 1.0, v160
	v_exp_f32_e32 v131, v215
	v_exp_f32_e32 v132, v214
	v_exp_f32_e32 v133, v213
	v_exp_f32_e32 v220, v212
	v_add_f32_e32 v134, 1.0, v161
	v_add_f32_e32 v135, 1.0, v193
	v_add_f32_e32 v136, 1.0, v217
	v_mfma_f32_32x32x16_bf16 v[2:17], v[42:45], v[138:141], v[2:17]
	ds_read_b128 v[158:161], v192 offset:16416
	v_fmac_f32_e32 v130, v130, v131
	v_fmac_f32_e32 v134, v134, v132
	v_fmac_f32_e32 v135, v135, v133
	v_fmac_f32_e32 v136, v136, v220
	v_mfma_f32_32x32x16_bf16 v[2:17], v[38:41], v[146:149], v[2:17]
	ds_read_b128 v[186:189], v192 offset:16448
	v_rcp_f32_e32 v130, v130
	v_rcp_f32_e32 v134, v134
	v_mfma_f32_32x32x16_bf16 v[2:17], v[34:37], v[150:153], v[2:17]
	ds_read_b128 v[190:193], v192 offset:16480
	v_rcp_f32_e32 v135, v135
	v_rcp_f32_e32 v136, v136
	v_fma_f32 v130, -v131, v130, v130
	v_fma_f32 v131, -v132, v134, v134
	s_waitcnt lgkmcnt(4)
	v_mfma_f32_32x32x16_bf16 v[18:33], v[126:129], v[194:197], v[18:33]
	v_fma_f32 v132, -v133, v135, v135
	v_fma_f32 v133, -v220, v136, v136
	v_cvt_pk_bf16_f32 v252, v130, v131
	v_cvt_pk_bf16_f32 v253, v132, v133
	v_mfma_f32_32x32x16_bf16 v[18:33], v[122:125], v[178:181], v[18:33]
	s_nop 1
	v_exp_f32_e32 v131, v4
	v_exp_f32_e32 v130, v8
	v_exp_f32_e32 v133, v12
	v_exp_f32_e32 v132, v16
	v_mfma_f32_32x32x16_bf16 v[18:33], v[118:121], v[170:173], v[18:33]
	v_exp_f32_e32 v2, v2
	v_exp_f32_e32 v6, v6
	v_exp_f32_e32 v10, v10
	v_exp_f32_e32 v12, v14
	v_fma_f32 v4, v131, s12, s12
	v_fma_f32 v8, v130, s12, s12
	v_fma_f32 v14, v133, s12, s12
	v_fma_f32 v16, v132, s12, s12
	v_mfma_f32_32x32x16_bf16 v[18:33], v[114:117], v[166:169], v[18:33]
	v_exp_f32_e32 v3, v3
	v_fmac_f32_e32 v4, v2, v4
	v_exp_f32_e32 v2, v7
	v_fmac_f32_e32 v8, v6, v8
	v_exp_f32_e32 v6, v11
	v_exp_f32_e32 v7, v15
	v_fmac_f32_e32 v14, v10, v14
	v_fmac_f32_e32 v16, v12, v16
	v_mfma_f32_32x32x16_bf16 v[18:33], v[110:113], v[162:165], v[18:33]
	v_add_f32_e32 v10, 1.0, v3
	v_rcp_f32_e32 v3, v4
	v_add_f32_e32 v4, 1.0, v2
	v_rcp_f32_e32 v2, v8
	v_rcp_f32_e32 v135, v14
	v_rcp_f32_e32 v134, v16
	v_mfma_f32_32x32x16_bf16 v[18:33], v[106:109], v[174:177], v[18:33]
	v_add_f32_e32 v6, 1.0, v6
	v_add_f32_e32 v7, 1.0, v7
	v_rcp_f32_e32 v137, v10
	v_rcp_f32_e32 v136, v4
	v_exp_f32_e32 v140, v5
	v_exp_f32_e32 v141, v9
	v_mfma_f32_32x32x16_bf16 v[18:33], v[102:105], v[182:185], v[18:33]
	v_rcp_f32_e32 v139, v6
	v_rcp_f32_e32 v138, v7
	v_exp_f32_e32 v146, v13
	v_exp_f32_e32 v147, v17
	v_mfma_f32_32x32x16_bf16 v[18:33], v[98:101], v[142:145], v[18:33]
	v_fma_f32 v130, -v130, v2, v2
	v_fma_f32 v131, -v131, v3, v3
	v_pk_fma_f32 v[224:225], v[136:137], v[204:205], v[130:131]
	s_nop 0
	v_pk_fma_f32 v[130:131], v[132:133], v[134:135], v[134:135] neg_lo:[1,0,0] neg_hi:[1,0,0]
	s_nop 0
	v_pk_fma_f32 v[226:227], v[138:139], v[202:203], v[130:131]
	s_waitcnt lgkmcnt(0)
	v_mfma_f32_32x32x16_bf16 v[18:33], v[94:97], v[154:157], v[18:33]
	v_add_f32_e32 v130, 1.0, v140
	v_exp_f32_e32 v131, v225
	v_add_f32_e32 v132, 1.0, v141
	v_exp_f32_e32 v133, v224
	v_exp_f32_e32 v134, v227
	v_exp_f32_e32 v135, v226
	v_add_f32_e32 v136, 1.0, v146
	v_add_f32_e32 v137, 1.0, v147
	v_mfma_f32_32x32x16_bf16 v[18:33], v[90:93], v[158:161], v[18:33]
	v_fmac_f32_e32 v130, v130, v131
	v_fmac_f32_e32 v132, v132, v133
	v_fmac_f32_e32 v136, v136, v134
	v_fmac_f32_e32 v137, v137, v135
	v_rcp_f32_e32 v130, v130
	v_rcp_f32_e32 v132, v132
	v_mfma_f32_32x32x16_bf16 v[18:33], v[86:89], v[186:189], v[18:33]
	v_rcp_f32_e32 v136, v136
	v_rcp_f32_e32 v137, v137
	v_fma_f32 v130, -v131, v130, v130
	v_fma_f32 v131, -v133, v132, v132
	v_mfma_f32_32x32x16_bf16 v[18:33], v[82:85], v[190:193], v[18:33]
	v_fma_f32 v132, -v134, v136, v136
	v_fma_f32 v133, -v135, v137, v137
	v_cvt_pk_bf16_f32 v254, v130, v131
	v_cvt_pk_bf16_f32 v255, v132, v133
	ds_write_b128 v211, v[252:255] offset:0
	s_waitcnt lgkmcnt(0)
	s_barrier
	v_mfma_f32_32x32x16_bf16 v[2:17], v[78:81], v[194:197], v[236:251]
	ds_read_b128 v[202:205], v210
	v_add_u32_e32 v216, v230, v228
	v_mfma_f32_32x32x16_bf16 v[2:17], v[74:77], v[178:181], v[2:17]
	ds_read_b128 v[194:197], v210 offset:1024
	v_exp_f32_e32 v147, v20
	v_exp_f32_e32 v146, v24
	v_exp_f32_e32 v149, v28
	v_exp_f32_e32 v148, v32
	v_mfma_f32_32x32x16_bf16 v[2:17], v[70:73], v[170:173], v[2:17]
	ds_read_b128 v[138:141], v210 offset:2048
	v_exp_f32_e32 v18, v18
	v_exp_f32_e32 v22, v22
	v_exp_f32_e32 v24, v26
	v_exp_f32_e32 v26, v30
	v_fma_f32 v20, v147, s12, s12
	v_fma_f32 v28, v146, s12, s12
	v_fma_f32 v30, v149, s12, s12
	v_fma_f32 v32, v148, s12, s12
	v_mfma_f32_32x32x16_bf16 v[2:17], v[66:69], v[166:169], v[2:17]
	ds_read_b128 v[134:137], v210 offset:3072
	v_exp_f32_e32 v19, v19
	v_exp_f32_e32 v23, v23
	v_exp_f32_e32 v27, v27
	v_exp_f32_e32 v31, v31
	v_fmac_f32_e32 v20, v18, v20
	v_fmac_f32_e32 v28, v22, v28
	v_fmac_f32_e32 v30, v24, v30
	v_fmac_f32_e32 v32, v26, v32
	v_mfma_f32_32x32x16_bf16 v[2:17], v[62:65], v[162:165], v[2:17]
	ds_read_b128 v[166:169], v210 offset:4096
	v_add_f32_e32 v22, 1.0, v19
	v_rcp_f32_e32 v19, v20
	v_rcp_f32_e32 v18, v28
	v_rcp_f32_e32 v151, v30
	v_rcp_f32_e32 v150, v32
	v_add_f32_e32 v20, 1.0, v23
	v_mfma_f32_32x32x16_bf16 v[2:17], v[58:61], v[174:177], v[2:17]
	ds_read_b128 v[162:165], v210 offset:5120
	v_rcp_f32_e32 v153, v22
	v_rcp_f32_e32 v152, v20
	v_add_f32_e32 v23, 1.0, v27
	v_add_f32_e32 v20, 1.0, v31
	v_exp_f32_e32 v180, v21
	v_exp_f32_e32 v181, v25
	v_mfma_f32_32x32x16_bf16 v[2:17], v[54:57], v[182:185], v[2:17]
	ds_read_b128 v[170:173], v210 offset:6144
	v_rcp_f32_e32 v175, v23
	v_rcp_f32_e32 v174, v20
	v_exp_f32_e32 v176, v29
	v_exp_f32_e32 v177, v33
	v_mfma_f32_32x32x16_bf16 v[2:17], v[50:53], v[142:145], v[2:17]
	ds_read_b128 v[130:133], v210 offset:7168
	v_fma_f32 v146, -v146, v18, v18
	v_fma_f32 v147, -v147, v19, v19
	ds_read_b128 v[18:21], v231 offset:36928
	ds_read_b128 v[22:25], v231 offset:36944
	ds_read_b128 v[26:29], v231 offset:36960
	ds_read_b128 v[30:33], v231 offset:36976
	v_pk_fma_f32 v[220:221], v[152:153], v[200:201], v[146:147]
	v_pk_fma_f32 v[142:143], v[148:149], v[150:151], v[150:151] neg_lo:[1,0,0] neg_hi:[1,0,0]
	s_nop 0
	v_pk_fma_f32 v[222:223], v[174:175], v[198:199], v[142:143]
	v_mfma_f32_32x32x16_bf16 v[2:17], v[46:49], v[154:157], v[2:17]
	ds_read_b128 v[146:149], v216 offset:16384
	v_add_f32_e32 v142, 1.0, v180
	v_exp_f32_e32 v143, v221
	v_exp_f32_e32 v144, v220
	v_exp_f32_e32 v145, v223
	v_exp_f32_e32 v180, v222
	v_add_f32_e32 v154, 1.0, v181
	v_add_f32_e32 v155, 1.0, v176
	v_add_f32_e32 v156, 1.0, v177
	v_mfma_f32_32x32x16_bf16 v[2:17], v[42:45], v[158:161], v[2:17]
	ds_read_b128 v[150:153], v216 offset:16416
	v_fmac_f32_e32 v142, v142, v143
	v_fmac_f32_e32 v154, v154, v144
	v_fmac_f32_e32 v155, v155, v145
	v_fmac_f32_e32 v156, v156, v180
	v_mfma_f32_32x32x16_bf16 v[2:17], v[38:41], v[186:189], v[2:17]
	ds_read_b128 v[174:177], v216 offset:16448
	v_rcp_f32_e32 v142, v142
	v_rcp_f32_e32 v154, v154
	v_mfma_f32_32x32x16_bf16 v[2:17], v[34:37], v[190:193], v[2:17]
	ds_read_b128 v[198:201], v216 offset:16480
	v_rcp_f32_e32 v155, v155
	v_rcp_f32_e32 v156, v156
	v_fma_f32 v142, -v143, v142, v142
	v_fma_f32 v143, -v144, v154, v154
	s_waitcnt lgkmcnt(4)
	v_mfma_f32_32x32x16_bf16 v[18:33], v[126:129], v[202:205], v[18:33]
	v_fma_f32 v144, -v145, v155, v155
	v_fma_f32 v145, -v180, v156, v156
	v_cvt_pk_bf16_f32 v252, v142, v143
	v_cvt_pk_bf16_f32 v253, v144, v145
	v_mfma_f32_32x32x16_bf16 v[18:33], v[122:125], v[194:197], v[18:33]
	s_nop 1
	v_exp_f32_e32 v143, v4
	v_exp_f32_e32 v142, v8
	v_exp_f32_e32 v145, v12
	v_exp_f32_e32 v144, v16
	v_mfma_f32_32x32x16_bf16 v[18:33], v[118:121], v[138:141], v[18:33]
	v_exp_f32_e32 v2, v2
	v_exp_f32_e32 v6, v6
	v_exp_f32_e32 v10, v10
	v_exp_f32_e32 v12, v14
	v_fma_f32 v4, v143, s12, s12
	v_fma_f32 v8, v142, s12, s12
	v_fma_f32 v14, v145, s12, s12
	v_fma_f32 v16, v144, s12, s12
	v_mfma_f32_32x32x16_bf16 v[18:33], v[114:117], v[134:137], v[18:33]
	v_exp_f32_e32 v3, v3
	v_fmac_f32_e32 v4, v2, v4
	v_exp_f32_e32 v2, v7
	v_fmac_f32_e32 v8, v6, v8
	v_exp_f32_e32 v6, v11
	v_exp_f32_e32 v7, v15
	v_fmac_f32_e32 v14, v10, v14
	v_fmac_f32_e32 v16, v12, v16
	v_mfma_f32_32x32x16_bf16 v[18:33], v[110:113], v[166:169], v[18:33]
	v_add_f32_e32 v10, 1.0, v3
	v_rcp_f32_e32 v3, v4
	v_add_f32_e32 v4, 1.0, v2
	v_rcp_f32_e32 v2, v8
	v_rcp_f32_e32 v155, v14
	v_rcp_f32_e32 v154, v16
	v_mfma_f32_32x32x16_bf16 v[18:33], v[106:109], v[162:165], v[18:33]
	v_add_f32_e32 v6, 1.0, v6
	v_add_f32_e32 v7, 1.0, v7
	v_rcp_f32_e32 v157, v10
	v_rcp_f32_e32 v156, v4
	v_exp_f32_e32 v160, v5
	v_exp_f32_e32 v161, v9
	v_mfma_f32_32x32x16_bf16 v[18:33], v[102:105], v[170:173], v[18:33]
	v_rcp_f32_e32 v159, v6
	v_rcp_f32_e32 v158, v7
	v_exp_f32_e32 v180, v13
	v_exp_f32_e32 v181, v17
	v_mfma_f32_32x32x16_bf16 v[18:33], v[98:101], v[130:133], v[18:33]
	v_fma_f32 v142, -v142, v2, v2
	v_fma_f32 v143, -v143, v3, v3
	v_pk_fma_f32 v[216:217], v[156:157], v[206:207], v[142:143]
	s_nop 0
	v_pk_fma_f32 v[142:143], v[144:145], v[154:155], v[154:155] neg_lo:[1,0,0] neg_hi:[1,0,0]
	s_nop 0
	v_pk_fma_f32 v[218:219], v[158:159], v[208:209], v[142:143]
	s_waitcnt lgkmcnt(0)
	v_mfma_f32_32x32x16_bf16 v[18:33], v[94:97], v[146:149], v[18:33]
	v_add_f32_e32 v142, 1.0, v160
	v_exp_f32_e32 v143, v217
	v_add_f32_e32 v144, 1.0, v161
	v_exp_f32_e32 v145, v216
	v_exp_f32_e32 v154, v219
	v_exp_f32_e32 v155, v218
	v_add_f32_e32 v156, 1.0, v180
	v_add_f32_e32 v157, 1.0, v181
	v_mfma_f32_32x32x16_bf16 v[18:33], v[90:93], v[150:153], v[18:33]
	v_fmac_f32_e32 v142, v142, v143
	v_fmac_f32_e32 v144, v144, v145
	v_fmac_f32_e32 v156, v156, v154
	v_fmac_f32_e32 v157, v157, v155
	v_rcp_f32_e32 v142, v142
	v_rcp_f32_e32 v144, v144
	v_mfma_f32_32x32x16_bf16 v[18:33], v[86:89], v[174:177], v[18:33]
	v_rcp_f32_e32 v156, v156
	v_rcp_f32_e32 v157, v157
	v_fma_f32 v142, -v143, v142, v142
	v_fma_f32 v143, -v145, v144, v144
	v_mfma_f32_32x32x16_bf16 v[18:33], v[82:85], v[198:201], v[18:33]
	v_fma_f32 v144, -v154, v156, v156
	v_fma_f32 v145, -v155, v157, v157
	v_cvt_pk_bf16_f32 v254, v142, v143
	v_cvt_pk_bf16_f32 v255, v144, v145
	ds_write_b128 v211, v[252:255] offset:8192
	s_waitcnt lgkmcnt(0)
	s_barrier
	v_mfma_f32_32x32x16_bf16 v[2:17], v[78:81], v[202:205], v[236:251]
	v_add_u32_e32 v234, v230, v229
	ds_read2_b32 v[228:229], v232 offset0:64 offset1:96
	ds_read_b128 v[206:209], v210 offset:8192
	v_mfma_f32_32x32x16_bf16 v[2:17], v[74:77], v[194:197], v[2:17]
	ds_read_b128 v[190:193], v210 offset:9216
	v_exp_f32_e32 v179, v20
	v_exp_f32_e32 v178, v24
	v_exp_f32_e32 v181, v28
	v_exp_f32_e32 v180, v32
	v_mfma_f32_32x32x16_bf16 v[2:17], v[70:73], v[138:141], v[2:17]
	ds_read_b128 v[158:161], v210 offset:10240
	v_exp_f32_e32 v18, v18
	v_exp_f32_e32 v22, v22
	v_exp_f32_e32 v24, v26
	v_exp_f32_e32 v26, v30
	v_fma_f32 v20, v179, s12, s12
	v_fma_f32 v28, v178, s12, s12
	v_fma_f32 v30, v181, s12, s12
	v_fma_f32 v32, v180, s12, s12
	v_mfma_f32_32x32x16_bf16 v[2:17], v[66:69], v[134:137], v[2:17]
	ds_read_b128 v[142:145], v210 offset:11264
	v_exp_f32_e32 v19, v19
	v_exp_f32_e32 v23, v23
	v_exp_f32_e32 v27, v27
	v_exp_f32_e32 v31, v31
	v_fmac_f32_e32 v20, v18, v20
	v_fmac_f32_e32 v28, v22, v28
	v_fmac_f32_e32 v30, v24, v30
	v_fmac_f32_e32 v32, v26, v32
	v_mfma_f32_32x32x16_bf16 v[2:17], v[62:65], v[166:169], v[2:17]
	ds_read_b128 v[154:157], v210 offset:12288
	v_add_f32_e32 v22, 1.0, v19
	v_rcp_f32_e32 v19, v20
	v_rcp_f32_e32 v18, v28
	v_rcp_f32_e32 v139, v30
	v_rcp_f32_e32 v138, v32
	v_add_f32_e32 v20, 1.0, v23
	v_mfma_f32_32x32x16_bf16 v[2:17], v[58:61], v[162:165], v[2:17]
	ds_read_b128 v[182:185], v210 offset:13312
	v_rcp_f32_e32 v141, v22
	v_rcp_f32_e32 v140, v20
	v_add_f32_e32 v23, 1.0, v27
	v_add_f32_e32 v20, 1.0, v31
	v_exp_f32_e32 v168, v21
	v_exp_f32_e32 v169, v25
	v_mfma_f32_32x32x16_bf16 v[2:17], v[54:57], v[170:173], v[2:17]
	ds_read_b128 v[186:189], v210 offset:14336
	v_rcp_f32_e32 v163, v23
	v_rcp_f32_e32 v162, v20
	v_exp_f32_e32 v194, v29
	v_exp_f32_e32 v195, v33
	v_mfma_f32_32x32x16_bf16 v[2:17], v[50:53], v[130:133], v[2:17]
	ds_read_b128 v[134:137], v210 offset:15360
	v_fma_f32 v166, -v178, v18, v18
	v_fma_f32 v167, -v179, v19, v19
	ds_read_b128 v[18:21], v231 offset:36928
	ds_read_b128 v[22:25], v231 offset:36944
	ds_read_b128 v[26:29], v231 offset:36960
	ds_read_b128 v[30:33], v231 offset:36976
	v_pk_fma_f32 v[214:215], v[140:141], v[214:215], v[166:167]
	v_pk_fma_f32 v[130:131], v[180:181], v[138:139], v[138:139] neg_lo:[1,0,0] neg_hi:[1,0,0]
	s_nop 0
	v_pk_fma_f32 v[212:213], v[162:163], v[212:213], v[130:131]
	v_mfma_f32_32x32x16_bf16 v[2:17], v[46:49], v[146:149], v[2:17]
	ds_read_b128 v[138:141], v234 offset:16384
	v_add_f32_e32 v130, 1.0, v168
	v_exp_f32_e32 v131, v215
	v_exp_f32_e32 v132, v214
	v_exp_f32_e32 v133, v213
	v_exp_f32_e32 v162, v212
	v_add_f32_e32 v163, 1.0, v169
	v_add_f32_e32 v166, 1.0, v194
	v_add_f32_e32 v167, 1.0, v195
	v_mfma_f32_32x32x16_bf16 v[2:17], v[42:45], v[150:153], v[2:17]
	ds_read_b128 v[146:149], v234 offset:16416
	v_fmac_f32_e32 v130, v130, v131
	v_fmac_f32_e32 v163, v163, v132
	v_fmac_f32_e32 v166, v166, v133
	v_fmac_f32_e32 v167, v167, v162
	v_mfma_f32_32x32x16_bf16 v[2:17], v[38:41], v[174:177], v[2:17]
	ds_read_b128 v[150:153], v234 offset:16448
	v_rcp_f32_e32 v130, v130
	v_rcp_f32_e32 v163, v163
	v_mfma_f32_32x32x16_bf16 v[2:17], v[34:37], v[198:201], v[2:17]
	ds_read_b128 v[178:181], v234 offset:16480
	v_rcp_f32_e32 v166, v166
	v_rcp_f32_e32 v167, v167
	v_fma_f32 v130, -v131, v130, v130
	v_fma_f32 v131, -v132, v163, v163
	s_waitcnt lgkmcnt(4)
	v_mfma_f32_32x32x16_bf16 v[18:33], v[126:129], v[206:209], v[18:33]
	v_fma_f32 v132, -v133, v166, v166
	v_fma_f32 v133, -v162, v167, v167
	v_cvt_pk_bf16_f32 v252, v130, v131
	v_cvt_pk_bf16_f32 v253, v132, v133
	v_mfma_f32_32x32x16_bf16 v[18:33], v[122:125], v[190:193], v[18:33]
	s_nop 1
	v_exp_f32_e32 v131, v4
	v_exp_f32_e32 v130, v8
	v_exp_f32_e32 v133, v12
	v_exp_f32_e32 v132, v16
	v_mfma_f32_32x32x16_bf16 v[18:33], v[118:121], v[158:161], v[18:33]
	v_exp_f32_e32 v2, v2
	v_exp_f32_e32 v6, v6
	v_exp_f32_e32 v10, v10
	v_exp_f32_e32 v12, v14
	v_fma_f32 v4, v131, s12, s12
	v_fma_f32 v8, v130, s12, s12
	v_fma_f32 v14, v133, s12, s12
	v_fma_f32 v16, v132, s12, s12
	v_mfma_f32_32x32x16_bf16 v[18:33], v[114:117], v[142:145], v[18:33]
	v_exp_f32_e32 v3, v3
	v_fmac_f32_e32 v4, v2, v4
	v_exp_f32_e32 v2, v7
	v_fmac_f32_e32 v8, v6, v8
	v_exp_f32_e32 v6, v11
	v_exp_f32_e32 v7, v15
	v_fmac_f32_e32 v14, v10, v14
	v_fmac_f32_e32 v16, v12, v16
	v_mfma_f32_32x32x16_bf16 v[18:33], v[110:113], v[154:157], v[18:33]
	v_add_f32_e32 v10, 1.0, v3
	v_rcp_f32_e32 v3, v4
	v_add_f32_e32 v4, 1.0, v2
	v_rcp_f32_e32 v2, v8
	v_rcp_f32_e32 v163, v14
	v_rcp_f32_e32 v162, v16
	v_mfma_f32_32x32x16_bf16 v[18:33], v[106:109], v[182:185], v[18:33]
	v_add_f32_e32 v6, 1.0, v6
	v_add_f32_e32 v7, 1.0, v7
	v_rcp_f32_e32 v167, v10
	v_rcp_f32_e32 v166, v4
	v_exp_f32_e32 v170, v5
	v_exp_f32_e32 v171, v9
	v_mfma_f32_32x32x16_bf16 v[18:33], v[102:105], v[186:189], v[18:33]
	v_rcp_f32_e32 v169, v6
	v_rcp_f32_e32 v168, v7
	v_exp_f32_e32 v172, v13
	v_exp_f32_e32 v173, v17
	v_mfma_f32_32x32x16_bf16 v[18:33], v[98:101], v[134:137], v[18:33]
	v_fma_f32 v130, -v130, v2, v2
	v_fma_f32 v131, -v131, v3, v3
	v_pk_fma_f32 v[204:205], v[166:167], v[224:225], v[130:131]
	s_nop 0
	v_pk_fma_f32 v[130:131], v[132:133], v[162:163], v[162:163] neg_lo:[1,0,0] neg_hi:[1,0,0]
	s_nop 0
	v_pk_fma_f32 v[202:203], v[168:169], v[226:227], v[130:131]
	s_waitcnt lgkmcnt(0)
	v_mfma_f32_32x32x16_bf16 v[18:33], v[94:97], v[138:141], v[18:33]
	v_add_f32_e32 v130, 1.0, v170
	v_exp_f32_e32 v131, v205
	v_add_f32_e32 v132, 1.0, v171
	v_exp_f32_e32 v133, v204
	v_exp_f32_e32 v162, v203
	v_exp_f32_e32 v163, v202
	v_add_f32_e32 v164, 1.0, v172
	v_add_f32_e32 v165, 1.0, v173
	v_mfma_f32_32x32x16_bf16 v[18:33], v[90:93], v[146:149], v[18:33]
	v_fmac_f32_e32 v130, v130, v131
	v_fmac_f32_e32 v132, v132, v133
	v_fmac_f32_e32 v164, v164, v162
	v_fmac_f32_e32 v165, v165, v163
	v_rcp_f32_e32 v130, v130
	v_rcp_f32_e32 v132, v132
	v_mfma_f32_32x32x16_bf16 v[18:33], v[86:89], v[150:153], v[18:33]
	v_rcp_f32_e32 v164, v164
	v_rcp_f32_e32 v165, v165
	v_fma_f32 v130, -v131, v130, v130
	v_fma_f32 v131, -v133, v132, v132
	v_mfma_f32_32x32x16_bf16 v[18:33], v[82:85], v[178:181], v[18:33]
	v_fma_f32 v132, -v162, v164, v164
	v_fma_f32 v133, -v163, v165, v165
	v_cvt_pk_bf16_f32 v254, v130, v131
	v_cvt_pk_bf16_f32 v255, v132, v133
	ds_write_b128 v211, v[252:255] offset:0
	s_waitcnt lgkmcnt(0)
	s_barrier
	s_branch .LBB1_13
